# P6 epilogue: DMA staging skipped in the second pass of each 8-token group (rows still resident), DMA wait behind first copy's loads
# speedup vs baseline: 1.0019x; 1.0012x over previous
.LBB0_975:
	s_add_i32 s0, s96, s35
	s_ashr_i32 s1, s0, 31
	s_lshr_b32 s1, s1, 19
	s_add_i32 s0, s0, s1
	s_ashr_i32 s2, s0, 13
	s_xor_b64 s[14:15], s[6:7], -1
	s_ashr_i32 s0, s2, 31
	s_add_u32 s1, s2, s87
	s_addc_u32 s0, s0, 0
	s_waitcnt vmcnt(0)
	v_lshlrev_b32_e32 v186, 6, v179
	v_lshl_add_u32 v185, v179, 4, s85
	v_mov_b32_e32 v187, 0
	s_mul_i32 s40, s1, 0x6000
	s_add_u32 s40, s70, s40
	s_addc_u32 s41, s71, 0
	s_add_u32 s42, s40, 0x5000
	s_addc_u32 s43, s41, 0
	s_add_u32 s40, s40, 0x18000
	s_addc_u32 s41, s41, 0
	v_mov_b32_e32 v188, 0x10000
	v_lshl_add_u32 v188, v179, 4, v188
	s_bitcmp1_b32 s96, 2
	s_cbranch_scc1 .Lp6_stage_done
	s_add_i32 m0, s85, 0
	s_nop 0
	global_load_lds_dwordx4 v186, s[16:17] offset:0
	s_add_i32 m0, s85, 1008
	s_nop 0
	global_load_lds_dwordx4 v186, s[16:17] offset:16
	s_add_i32 m0, s85, 2016
	s_nop 0
	global_load_lds_dwordx4 v186, s[16:17] offset:32
	s_add_i32 m0, s85, 3024
	s_nop 0
	global_load_lds_dwordx4 v186, s[16:17] offset:48
	s_add_i32 m0, s85, 4096
	s_nop 0
	global_load_lds_dwordx4 v186, s[28:29] offset:0
	s_add_i32 m0, s85, 5104
	s_nop 0
	global_load_lds_dwordx4 v186, s[28:29] offset:16
	s_add_i32 m0, s85, 6112
	s_nop 0
	global_load_lds_dwordx4 v186, s[28:29] offset:32
	s_add_i32 m0, s85, 7120
	s_nop 0
	global_load_lds_dwordx4 v186, s[28:29] offset:48
	s_add_i32 m0, s85, 8192
	s_nop 0
	global_load_lds_dwordx4 v186, s[12:13] offset:0
	s_add_i32 m0, s85, 9200
	s_nop 0
	global_load_lds_dwordx4 v186, s[12:13] offset:16
	s_add_i32 m0, s85, 10208
	s_nop 0
	global_load_lds_dwordx4 v186, s[12:13] offset:32
	s_add_i32 m0, s85, 11216
	s_nop 0
	global_load_lds_dwordx4 v186, s[12:13] offset:48
	s_add_i32 m0, s85, 12288
	s_nop 0
	global_load_lds_dwordx4 v186, s[90:91] offset:0
	s_add_i32 m0, s85, 13296
	s_nop 0
	global_load_lds_dwordx4 v186, s[90:91] offset:16
	s_add_i32 m0, s85, 14304
	s_nop 0
	global_load_lds_dwordx4 v186, s[90:91] offset:32
	s_add_i32 m0, s85, 15312
	s_nop 0
	global_load_lds_dwordx4 v186, s[90:91] offset:48
	s_mov_b32 m0, 65536
	s_nop 0
	global_load_lds_dwordx4 v186, s[42:43] offset:0
	s_mov_b32 m0, 66544
	s_nop 0
	global_load_lds_dwordx4 v186, s[42:43] offset:16
	s_mov_b32 m0, 67552
	s_nop 0
	global_load_lds_dwordx4 v186, s[42:43] offset:32
	s_mov_b32 m0, 68560
	s_nop 0
	global_load_lds_dwordx4 v186, s[42:43] offset:48
	s_mov_b32 m0, 69632
	s_nop 0
	global_load_lds_dwordx4 v186, s[40:41] offset:0
	s_mov_b32 m0, 70640
	s_nop 0
	global_load_lds_dwordx4 v186, s[40:41] offset:16
	s_mov_b32 m0, 71648
	s_nop 0
	global_load_lds_dwordx4 v186, s[40:41] offset:32
	s_mov_b32 m0, 72656
	s_nop 0
	global_load_lds_dwordx4 v186, s[40:41] offset:48
.Lp6_stage_done:
	v_readlane_b32 s40, v253, 62
	v_readlane_b32 s41, v253, 63
	s_lshl_b64 s[44:45], s[96:97], 12
	v_lshlrev_b32_e32 v2, 6, v179
	s_add_u32 s40, s40, s44
	s_addc_u32 s41, s41, s45
	s_add_u32 s40, s40, 0x1000
	s_addc_u32 s41, s41, 0
	global_load_dword v184, v2, s[40:41]
	s_add_u32 s40, s40, 0x1000
	s_addc_u32 s41, s41, 0
	global_load_dword v184, v2, s[40:41]
	s_add_u32 s40, s40, 0x1000
	s_addc_u32 s41, s41, 0
	global_load_dword v184, v2, s[40:41]
	v_mov_b32_e32 v1, v179
	s_mulk_i32 s0, 0x6000
	s_mul_hi_u32 s3, s1, 0x6000
	s_add_i32 s3, s3, s0
	s_mulk_i32 s1, 0x6000
	v_lshlrev_b32_e32 v20, 4, v1
	s_add_u32 s6, s70, s1
	v_readlane_b32 s36, v253, 60
	v_ashrrev_i32_e32 v21, 31, v20
	s_addc_u32 s7, s71, s3
	s_lshl_b64 s[0:1], s[96:97], 12
	v_readlane_b32 s38, v253, 62
	v_lshlrev_b64 v[22:23], 2, v[20:21]
	v_readlane_b32 s39, v253, 63
	s_add_u32 s20, s38, s0
	v_lshl_add_u64 v[68:69], s[6:7], 0, v[22:23]
	s_mov_b64 s[6:7], 0x5000
	s_addc_u32 s21, s39, s1
	v_lshl_add_u64 v[12:13], v[68:69], 0, s[6:7]
	s_lshl_b64 s[6:7], s[96:97], 3
	v_lshl_add_u64 v[32:33], s[20:21], 0, v[22:23]
	s_add_u32 s6, s64, s6
	s_addc_u32 s7, s65, s7
	s_nop 0
	global_load_dwordx2 v[72:73], v3, s[6:7]
	global_load_dwordx4 v[16:19], v[32:33], off
	global_load_dwordx4 v[24:27], v[32:33], off offset:16
	global_load_dwordx4 v[28:31], v[32:33], off offset:32
	s_nop 0
	global_load_dwordx4 v[32:35], v[32:33], off offset:48
	s_waitcnt vmcnt(8)
	ds_read_b128 v[4:7], v188 offset:3072
	ds_read_b128 v[8:11], v188 offset:2048
	ds_read_b128 v[12:15], v188 offset:1024
	v_lshl_add_u64 v[60:61], s[16:17], 0, v[22:23]
	v_lshl_add_u64 v[64:65], s[28:29], 0, v[22:23]
	v_add_co_u32_e32 v68, vcc, s18, v68
	ds_read_b128 v[36:39], v185 offset:7168
	ds_read_b128 v[40:43], v185 offset:3072
	ds_read_b128 v[44:47], v185 offset:2048
	ds_read_b128 v[48:51], v185 offset:6144
	ds_read_b128 v[52:55], v185 offset:5120
	ds_read_b128 v[56:59], v185 offset:1024
	s_nop 0
	ds_read_b128 v[60:63], v185 offset:0
	s_nop 0
	ds_read_b128 v[64:67], v185 offset:4096
	v_addc_co_u32_e32 v69, vcc, 0, v69, vcc
	ds_read_b128 v[68:71], v188 offset:0
	v_add_u32_e32 v142, 64, v183
	v_xor_b32_e32 v1, 1, v178
	v_xor_b32_e32 v2, 2, v178
	v_cmp_lt_i32_e32 vcc, v1, v142
	v_xor_b32_e32 v74, 4, v178
	v_readlane_b32 s20, v255, 42
	v_cndmask_b32_e32 v1, v178, v1, vcc
	v_cmp_lt_i32_e32 vcc, v2, v142
	v_readlane_b32 s22, v255, 44
	s_add_u32 s0, s30, s0
	v_cndmask_b32_e32 v75, v178, v2, vcc
	v_lshlrev_b32_e32 v2, 2, v1
	v_lshlrev_b32_e32 v1, 2, v75
	v_cmp_lt_i32_e32 vcc, v74, v142
	s_addc_u32 s1, s31, s1
	v_readlane_b32 s37, v253, 61
	v_readlane_b32 s40, v254, 0
	v_readlane_b32 s41, v254, 1
	v_readlane_b32 s42, v254, 2
	v_readlane_b32 s43, v254, 3
	v_readlane_b32 s44, v254, 4
	v_readlane_b32 s45, v254, 5
	v_readlane_b32 s46, v254, 6
	v_readlane_b32 s47, v254, 7
	v_readlane_b32 s48, v254, 8
	v_readlane_b32 s49, v254, 9
	v_readlane_b32 s50, v254, 10
	v_readlane_b32 s51, v254, 11
	v_readlane_b32 s21, v255, 43
	v_readlane_b32 s23, v255, 45
	s_waitcnt lgkmcnt(0)
	s_waitcnt vmcnt(5)
	v_pk_add_f32 v[12:13], v[12:13], 1.0 op_sel_hi:[1,0]
	v_pk_add_f32 v[14:15], v[14:15], 1.0 op_sel_hi:[1,0]
	s_waitcnt lgkmcnt(0)
	s_waitcnt vmcnt(3)
	v_pk_add_f32 v[18:19], v[18:19], v[72:73] op_sel_hi:[1,0] neg_lo:[0,1] neg_hi:[0,1]
	v_pk_add_f32 v[4:5], v[4:5], 1.0 op_sel_hi:[1,0]
	v_pk_mul_f32 v[18:19], v[72:73], v[18:19] op_sel:[1,0]
	s_waitcnt lgkmcnt(0)
	s_waitcnt vmcnt(0)
	v_pk_add_f32 v[32:33], v[32:33], v[72:73] op_sel_hi:[1,0] neg_lo:[0,1] neg_hi:[0,1]
	v_pk_add_f32 v[34:35], v[34:35], v[72:73] op_sel_hi:[1,0] neg_lo:[0,1] neg_hi:[0,1]
	v_pk_mul_f32 v[32:33], v[72:73], v[32:33] op_sel:[1,0]
	v_pk_mul_f32 v[34:35], v[72:73], v[34:35] op_sel:[1,0]
	s_waitcnt lgkmcnt(0)
	s_waitcnt vmcnt(0)
	v_pk_fma_f32 v[32:33], v[32:33], v[40:41], v[36:37]
	v_pk_fma_f32 v[34:35], v[34:35], v[42:43], v[38:39]
	v_pk_mul_f32 v[32:33], v[32:33], s[34:35] op_sel_hi:[1,0]
	v_pk_add_f32 v[6:7], v[6:7], 1.0 op_sel_hi:[1,0]
	v_pk_add_f32 v[24:25], v[24:25], v[72:73] op_sel_hi:[1,0] neg_lo:[0,1] neg_hi:[0,1]
	v_pk_mul_f32 v[34:35], v[34:35], s[34:35] op_sel_hi:[1,0]
	v_pk_fma_f32 v[42:43], v[138:139], v[4:5], v[32:33]
	s_waitcnt lgkmcnt(0)
	s_waitcnt vmcnt(0)
	v_pk_fma_f32 v[4:5], v[18:19], v[62:63], v[66:67]
	v_pk_add_f32 v[16:17], v[16:17], v[72:73] op_sel_hi:[1,0] neg_lo:[0,1] neg_hi:[0,1]
	v_pk_mul_f32 v[24:25], v[72:73], v[24:25] op_sel:[1,0]
	v_pk_fma_f32 v[40:41], v[140:141], v[6:7], v[34:35]
	v_pk_mul_f32 v[4:5], v[4:5], s[34:35] op_sel_hi:[1,0]
	s_waitcnt lgkmcnt(0)
	s_waitcnt vmcnt(0)
	v_pk_add_f32 v[6:7], v[70:71], 1.0 op_sel_hi:[1,0]
	v_pk_fma_f32 v[24:25], v[24:25], v[56:57], v[52:53]
	v_pk_fma_f32 v[52:53], v[128:129], v[6:7], v[4:5]
	v_pk_mul_f32 v[4:5], v[72:73], v[16:17] op_sel:[1,0]
	v_pk_add_f32 v[26:27], v[26:27], v[72:73] op_sel_hi:[1,0] neg_lo:[0,1] neg_hi:[0,1]
	v_pk_fma_f32 v[4:5], v[60:61], v[4:5], v[64:65]
	v_pk_mul_f32 v[26:27], v[72:73], v[26:27] op_sel:[1,0]
	v_pk_mul_f32 v[4:5], v[4:5], s[34:35] op_sel_hi:[1,0]
	v_pk_add_f32 v[6:7], v[68:69], 1.0 op_sel_hi:[1,0]
	v_pk_fma_f32 v[26:27], v[26:27], v[58:59], v[54:55]
	v_pk_fma_f32 v[54:55], v[126:127], v[6:7], v[4:5]
	v_pk_add_f32 v[30:31], v[30:31], v[72:73] op_sel_hi:[1,0] neg_lo:[0,1] neg_hi:[0,1]
	v_add_f32_e32 v4, 0, v54
	v_add_f32_e32 v4, v4, v55
	v_pk_mul_f32 v[30:31], v[72:73], v[30:31] op_sel:[1,0]
	v_pk_mul_f32 v[24:25], v[24:25], s[34:35] op_sel_hi:[1,0]
	v_add_f32_e32 v4, v4, v52
	v_pk_add_f32 v[28:29], v[28:29], v[72:73] op_sel_hi:[1,0] neg_lo:[0,1] neg_hi:[0,1]
	v_pk_fma_f32 v[30:31], v[30:31], v[46:47], v[50:51]
	v_pk_fma_f32 v[50:51], v[130:131], v[12:13], v[24:25]
	v_add_f32_e32 v4, v4, v53
	v_pk_mul_f32 v[28:29], v[72:73], v[28:29] op_sel:[1,0]
	v_pk_mul_f32 v[26:27], v[26:27], s[34:35] op_sel_hi:[1,0]
	v_add_f32_e32 v4, v4, v50
	v_pk_fma_f32 v[28:29], v[28:29], v[44:45], v[48:49]
	v_pk_fma_f32 v[48:49], v[132:133], v[14:15], v[26:27]
	v_add_f32_e32 v4, v4, v51
	v_pk_add_f32 v[8:9], v[8:9], 1.0 op_sel_hi:[1,0]
	v_pk_mul_f32 v[28:29], v[28:29], s[34:35] op_sel_hi:[1,0]
	v_add_f32_e32 v4, v4, v48
	v_pk_fma_f32 v[46:47], v[134:135], v[8:9], v[28:29]
	v_add_f32_e32 v4, v4, v49
	v_pk_add_f32 v[10:11], v[10:11], 1.0 op_sel_hi:[1,0]
	v_pk_mul_f32 v[30:31], v[30:31], s[34:35] op_sel_hi:[1,0]
	v_add_f32_e32 v4, v4, v46
	v_pk_fma_f32 v[44:45], v[136:137], v[10:11], v[30:31]
	v_add_f32_e32 v4, v4, v47
	v_add_f32_e32 v4, v4, v44
	v_add_f32_e32 v4, v4, v45
	v_add_f32_e32 v4, v4, v42
	v_add_f32_e32 v4, v4, v43
	v_add_f32_e32 v4, v4, v40
	v_add_f32_e32 v4, v4, v41
	ds_bpermute_b32 v5, v2, v4
	v_cndmask_b32_e32 v6, v178, v74, vcc
	v_lshlrev_b32_e32 v74, 2, v6
	v_xor_b32_e32 v6, 8, v178
	v_cmp_lt_i32_e32 vcc, v6, v142
	s_waitcnt lgkmcnt(0)
	v_add_f32_e32 v4, v4, v5
	ds_bpermute_b32 v5, v1, v4
	v_cndmask_b32_e32 v6, v178, v6, vcc
	v_lshlrev_b32_e32 v75, 2, v6
	v_xor_b32_e32 v6, 16, v178
	v_cmp_lt_i32_e32 vcc, v6, v142
	s_waitcnt lgkmcnt(0)
	v_add_f32_e32 v4, v4, v5
	ds_bpermute_b32 v5, v74, v4
	v_cndmask_b32_e32 v6, v178, v6, vcc
	v_lshlrev_b32_e32 v126, 2, v6
	v_xor_b32_e32 v6, 32, v178
	v_cmp_lt_i32_e32 vcc, v6, v142
	s_waitcnt lgkmcnt(0)
	v_add_f32_e32 v7, v4, v5
	ds_bpermute_b32 v8, v75, v7
	v_cndmask_b32_e32 v4, v178, v6, vcc
	v_lshlrev_b32_e32 v127, 2, v4
	v_lshl_add_u64 v[4:5], s[12:13], 0, v[22:23]
	v_lshl_add_u64 v[36:37], s[90:91], 0, v[22:23]
	s_waitcnt lgkmcnt(0)
	v_add_f32_e32 v24, v7, v8
	ds_bpermute_b32 v25, v126, v24
	ds_read_b128 v[16:19], v185 offset:11264
	ds_read_b128 v[12:15], v185 offset:10240
	ds_read_b128 v[8:11], v185 offset:9216
	s_nop 0
	ds_read_b128 v[4:7], v185 offset:8192
	v_lshl_add_u64 v[22:23], s[0:1], 0, v[22:23]
	v_readlane_b32 s0, v255, 23
	v_readlane_b32 s1, v255, 24
	s_waitcnt lgkmcnt(0)
	v_add_f32_e32 v56, v24, v25
	ds_read_b128 v[24:27], v185 offset:15360
	ds_read_b128 v[28:31], v185 offset:14336
	ds_read_b128 v[32:35], v185 offset:13312
	s_nop 0
	ds_read_b128 v[36:39], v185 offset:12288
	ds_bpermute_b32 v57, v127, v56
	s_waitcnt lgkmcnt(0)
	v_add_f32_e32 v56, v56, v57
	v_mul_f32_e32 v56, 0x3a800000, v56
	v_pk_add_f32 v[54:55], v[54:55], v[56:57] op_sel_hi:[1,0] neg_lo:[0,1] neg_hi:[0,1]
	v_pk_add_f32 v[52:53], v[52:53], v[56:57] op_sel_hi:[1,0] neg_lo:[0,1] neg_hi:[0,1]
	v_pk_mul_f32 v[58:59], v[54:55], v[54:55]
	v_pk_mul_f32 v[60:61], v[52:53], v[52:53]
	v_add_f32_e32 v58, v58, v59
	v_pk_add_f32 v[50:51], v[50:51], v[56:57] op_sel_hi:[1,0] neg_lo:[0,1] neg_hi:[0,1]
	v_add_f32_e32 v58, v60, v58
	v_pk_mul_f32 v[62:63], v[50:51], v[50:51]
	v_add_f32_e32 v58, v61, v58
	v_pk_add_f32 v[48:49], v[48:49], v[56:57] op_sel_hi:[1,0] neg_lo:[0,1] neg_hi:[0,1]
	v_add_f32_e32 v58, v62, v58
	v_pk_mul_f32 v[64:65], v[48:49], v[48:49]
	v_add_f32_e32 v58, v63, v58
	v_pk_add_f32 v[46:47], v[46:47], v[56:57] op_sel_hi:[1,0] neg_lo:[0,1] neg_hi:[0,1]
	v_add_f32_e32 v58, v64, v58
	v_pk_mul_f32 v[66:67], v[46:47], v[46:47]
	v_add_f32_e32 v58, v65, v58
	v_pk_add_f32 v[44:45], v[44:45], v[56:57] op_sel_hi:[1,0] neg_lo:[0,1] neg_hi:[0,1]
	v_add_f32_e32 v58, v66, v58
	v_pk_mul_f32 v[68:69], v[44:45], v[44:45]
	v_add_f32_e32 v58, v67, v58
	v_pk_add_f32 v[42:43], v[42:43], v[56:57] op_sel_hi:[1,0] neg_lo:[0,1] neg_hi:[0,1]
	v_add_f32_e32 v58, v68, v58
	v_pk_mul_f32 v[70:71], v[42:43], v[42:43]
	v_add_f32_e32 v58, v69, v58
	v_pk_add_f32 v[40:41], v[40:41], v[56:57] op_sel_hi:[1,0] neg_lo:[0,1] neg_hi:[0,1]
	v_add_f32_e32 v58, v70, v58
	v_pk_mul_f32 v[56:57], v[40:41], v[40:41]
	v_add_f32_e32 v58, v71, v58
	v_add_f32_e32 v56, v56, v58
	v_add_f32_e32 v56, v57, v56
	ds_bpermute_b32 v57, v2, v56
	s_waitcnt lgkmcnt(0)
	v_add_f32_e32 v56, v56, v57
	ds_bpermute_b32 v57, v1, v56
	s_waitcnt lgkmcnt(0)
	v_add_f32_e32 v56, v56, v57
	ds_bpermute_b32 v57, v74, v56
	s_waitcnt lgkmcnt(0)
	v_add_f32_e32 v56, v56, v57
	ds_bpermute_b32 v57, v75, v56
	s_waitcnt lgkmcnt(0)
	v_add_f32_e32 v56, v56, v57
	ds_bpermute_b32 v57, v126, v56
	s_waitcnt lgkmcnt(0)
	v_add_f32_e32 v56, v56, v57
	ds_bpermute_b32 v57, v127, v56
	s_waitcnt lgkmcnt(0)
	v_add_f32_e32 v56, v56, v57
	v_fmamk_f32 v56, v56, 0x3a800000, v204
	v_mul_f32_e32 v57, 0x4b800000, v56
	v_cmp_gt_f32_e32 vcc, s22, v56
	s_nop 1
	v_cndmask_b32_e32 v56, v56, v57, vcc
	v_rsq_f32_e32 v56, v56
	s_nop 0
	v_mul_f32_e32 v57, 0x45800000, v56
	v_cndmask_b32_e32 v56, v56, v57, vcc
	v_pk_mul_f32 v[54:55], v[54:55], v[56:57] op_sel_hi:[1,0]
	v_pk_mul_f32 v[52:53], v[52:53], v[56:57] op_sel_hi:[1,0]
	s_waitcnt lgkmcnt(0)
	s_waitcnt vmcnt(0)
	v_pk_fma_f32 v[4:5], v[4:5], v[54:55], v[36:37]
	v_pk_mul_f32 v[36:37], v[50:51], v[56:57] op_sel_hi:[1,0]
	v_pk_fma_f32 v[6:7], v[6:7], v[52:53], v[38:39]
	v_pk_fma_f32 v[8:9], v[8:9], v[36:37], v[32:33]
	v_pk_mul_f32 v[32:33], v[48:49], v[56:57] op_sel_hi:[1,0]
	s_and_b64 vcc, exec, s[0:1]
	v_pk_fma_f32 v[10:11], v[10:11], v[32:33], v[34:35]
	v_pk_mul_f32 v[32:33], v[46:47], v[56:57] op_sel_hi:[1,0]
	s_nop 0
	v_pk_fma_f32 v[12:13], v[12:13], v[32:33], v[28:29]
	v_pk_mul_f32 v[28:29], v[44:45], v[56:57] op_sel_hi:[1,0]
	s_nop 0
	v_pk_fma_f32 v[14:15], v[14:15], v[28:29], v[30:31]
	v_pk_mul_f32 v[28:29], v[42:43], v[56:57] op_sel_hi:[1,0]
	s_nop 0
	v_pk_fma_f32 v[16:17], v[16:17], v[28:29], v[24:25]
	v_pk_mul_f32 v[24:25], v[40:41], v[56:57] op_sel_hi:[1,0]
	s_nop 0
	v_pk_fma_f32 v[18:19], v[18:19], v[24:25], v[26:27]
	global_store_dwordx4 v[22:23], v[4:7], off
	global_store_dwordx4 v[22:23], v[8:11], off offset:16
	global_store_dwordx4 v[22:23], v[12:15], off offset:32
	global_store_dwordx4 v[22:23], v[16:19], off offset:48
	s_cbranch_vccz .LBB0_977
	s_lshl_b64 s[0:1], s[96:97], 10
	s_mul_hi_i32 s3, s2, 0x6000
	s_mulk_i32 s2, 0x6000
	s_add_u32 s2, s70, s2
	s_addc_u32 s3, s71, s3
	v_lshl_add_u64 v[50:51], v[20:21], 2, s[2:3]
	s_mov_b64 s[2:3], 0x19000
	v_add_co_u32_e32 v34, vcc, s86, v50
	v_lshl_add_u64 v[30:31], v[50:51], 0, s[2:3]
	s_mov_b64 s[2:3], 0x18000
	v_addc_co_u32_e32 v35, vcc, 0, v51, vcc
	v_lshl_add_u64 v[46:47], v[50:51], 0, s[2:3]
	v_add_co_u32_e32 v50, vcc, s67, v50
	global_load_dwordx4 v[22:25], v[30:31], off offset:32
	global_load_dwordx4 v[26:29], v[30:31], off offset:16
	v_addc_co_u32_e32 v51, vcc, 0, v51, vcc
	global_load_dwordx4 v[30:33], v[30:31], off offset:48
	s_nop 0
	global_load_dwordx4 v[34:37], v[34:35], off
	s_nop 0
	ds_read_b128 v[38:41], v188 offset:5120
	ds_read_b128 v[42:45], v188 offset:7168
	s_nop 0
	ds_read_b128 v[46:49], v188 offset:6144
	s_lshl_b64 s[0:1], s[0:1], 1
	ds_read_b128 v[50:53], v188 offset:4096
	s_add_u32 s0, s76, s0
	s_addc_u32 s1, s77, s1
	v_lshl_add_u64 v[20:21], v[20:21], 1, s[0:1]
	s_waitcnt lgkmcnt(0)
	s_waitcnt vmcnt(3)
	v_pk_add_f32 v[22:23], v[22:23], 1.0 op_sel_hi:[1,0]
	s_waitcnt lgkmcnt(0)
	s_waitcnt vmcnt(2)
	v_pk_add_f32 v[26:27], v[26:27], 1.0 op_sel_hi:[1,0]
	v_pk_add_f32 v[28:29], v[28:29], 1.0 op_sel_hi:[1,0]
	s_waitcnt lgkmcnt(0)
	s_waitcnt vmcnt(0)
	v_pk_add_f32 v[34:35], v[34:35], 1.0 op_sel_hi:[1,0]
	v_pk_add_f32 v[36:37], v[36:37], 1.0 op_sel_hi:[1,0]
	v_pk_add_f32 v[24:25], v[24:25], 1.0 op_sel_hi:[1,0]
	v_pk_add_f32 v[30:31], v[30:31], 1.0 op_sel_hi:[1,0]
	v_pk_add_f32 v[32:33], v[32:33], 1.0 op_sel_hi:[1,0]
	s_waitcnt lgkmcnt(0)
	s_waitcnt vmcnt(0)
	v_pk_fma_f32 v[8:9], v[8:9], v[26:27], v[38:39]
	v_pk_fma_f32 v[10:11], v[10:11], v[28:29], v[40:41]
	s_waitcnt lgkmcnt(0)
	s_waitcnt vmcnt(0)
	v_pk_fma_f32 v[12:13], v[12:13], v[22:23], v[46:47]
	s_waitcnt lgkmcnt(0)
	s_waitcnt vmcnt(0)
	v_pk_fma_f32 v[4:5], v[4:5], v[34:35], v[50:51]
	v_pk_fma_f32 v[22:23], v[6:7], v[36:37], v[52:53]
	v_pk_fma_f32 v[14:15], v[14:15], v[24:25], v[48:49]
	v_pk_fma_f32 v[16:17], v[16:17], v[30:31], v[42:43]
	v_pk_fma_f32 v[18:19], v[18:19], v[32:33], v[44:45]
	v_cvt_pk_bf16_f32 v6, v8, v9
	v_cvt_pk_bf16_f32 v7, v10, v11
	v_cvt_pk_bf16_f32 v4, v4, v5
	v_cvt_pk_bf16_f32 v5, v22, v23
	v_cvt_pk_bf16_f32 v8, v12, v13
	v_cvt_pk_bf16_f32 v9, v14, v15
	v_cvt_pk_bf16_f32 v10, v16, v17
	v_cvt_pk_bf16_f32 v11, v18, v19
	global_store_dwordx4 v[20:21], v[4:7], off
	global_store_dwordx4 v[20:21], v[8:11], off offset:16
